# grid-barrier release flattening: non-leader WGs poll cross-XCD generation word directly, skipping per-XCD relay hop (on v16)
# baseline (speedup 1.0000x reference)
.LBB0_87:
	s_or_b64 exec, exec, s[28:29]
	v_cvt_f32_u32_e32 v5, v3
	s_waitcnt vmcnt(0)
	v_readfirstlane_b32 s4, v4
	v_sub_u32_e32 v4, 0, v3
	v_rcp_iflag_f32_e32 v5, v5
	v_add_u32_e32 v6, s4, v1
	v_mul_f32_e32 v5, 0x4f7ffffe, v5
	v_cvt_u32_f32_e32 v5, v5
	v_mul_lo_u32 v1, v4, v5
	v_mul_hi_u32 v1, v5, v1
	v_add_u32_e32 v1, v5, v1
	v_mul_hi_u32 v1, v6, v1
	v_mul_lo_u32 v4, v1, v3
	v_sub_u32_e32 v4, v6, v4
	v_add_u32_e32 v5, 1, v1
	v_cmp_ge_u32_e32 vcc, v4, v3
	s_nop 1
	v_cndmask_b32_e32 v1, v1, v5, vcc
	v_sub_u32_e32 v5, v4, v3
	v_cndmask_b32_e32 v4, v4, v5, vcc
	v_add_u32_e32 v5, 1, v1
	v_cmp_ge_u32_e32 vcc, v4, v3
	v_add_u32_e32 v4, 1, v6
	s_nop 0
	v_cndmask_b32_e32 v1, v1, v5, vcc
	v_mul_lo_u32 v5, v3, v1
	v_add_u32_e32 v3, v5, v3
	v_cmp_ne_u32_e32 vcc, v4, v3
	s_and_saveexec_b64 s[4:5], vcc
	s_xor_b64 s[28:29], exec, s[4:5]
	s_cbranch_execz .LBB0_101
	v_readlane_b32 s4, v254, 49
	v_readlane_b32 s5, v254, 50
	s_waitcnt lgkmcnt(0)
	s_nop 3
	global_load_dword v2, v115, s[4:5] sc1
	s_waitcnt vmcnt(0)
	v_cmp_eq_u32_e32 vcc, v2, v1
	s_and_saveexec_b64 s[38:39], vcc
	s_cbranch_execz .LBB0_100
	s_mov_b32 s4, 1
	s_mov_b64 s[40:41], 0
	s_branch .LBB0_91

.LBB0_238:
	s_or_b64 exec, exec, s[26:27]
	v_cvt_f32_u32_e32 v5, v3
	s_waitcnt vmcnt(0)
	v_readfirstlane_b32 s4, v4
	v_sub_u32_e32 v4, 0, v3
	v_rcp_iflag_f32_e32 v5, v5
	v_add_u32_e32 v6, s4, v1
	v_mul_f32_e32 v5, 0x4f7ffffe, v5
	v_cvt_u32_f32_e32 v5, v5
	v_mul_lo_u32 v1, v4, v5
	v_mul_hi_u32 v1, v5, v1
	v_add_u32_e32 v1, v5, v1
	v_mul_hi_u32 v1, v6, v1
	v_mul_lo_u32 v4, v1, v3
	v_sub_u32_e32 v4, v6, v4
	v_add_u32_e32 v5, 1, v1
	v_cmp_ge_u32_e32 vcc, v4, v3
	s_nop 1
	v_cndmask_b32_e32 v1, v1, v5, vcc
	v_sub_u32_e32 v5, v4, v3
	v_cndmask_b32_e32 v4, v4, v5, vcc
	v_add_u32_e32 v5, 1, v1
	v_cmp_ge_u32_e32 vcc, v4, v3
	v_add_u32_e32 v4, 1, v6
	s_nop 0
	v_cndmask_b32_e32 v1, v1, v5, vcc
	v_mul_lo_u32 v5, v3, v1
	v_add_u32_e32 v3, v5, v3
	v_cmp_ne_u32_e32 vcc, v4, v3
	s_and_saveexec_b64 s[4:5], vcc
	s_xor_b64 s[26:27], exec, s[4:5]
	s_cbranch_execz .LBB0_252
	v_readlane_b32 s4, v254, 49
	v_readlane_b32 s5, v254, 50
	s_waitcnt lgkmcnt(0)
	s_nop 3
	global_load_dword v2, v115, s[4:5] sc1
	s_waitcnt vmcnt(0)
	v_cmp_eq_u32_e32 vcc, v2, v1
	s_and_saveexec_b64 s[28:29], vcc
	s_cbranch_execz .LBB0_251
	s_mov_b32 s4, 1
	s_mov_b64 s[38:39], 0
	s_branch .LBB0_242

.LBB0_413:
	s_or_b64 exec, exec, s[10:11]
	v_cvt_f32_u32_e32 v5, v3
	s_waitcnt vmcnt(0)
	v_readfirstlane_b32 s4, v4
	v_sub_u32_e32 v4, 0, v3
	v_rcp_iflag_f32_e32 v5, v5
	v_add_u32_e32 v6, s4, v1
	v_mul_f32_e32 v5, 0x4f7ffffe, v5
	v_cvt_u32_f32_e32 v5, v5
	v_mul_lo_u32 v1, v4, v5
	v_mul_hi_u32 v1, v5, v1
	v_add_u32_e32 v1, v5, v1
	v_mul_hi_u32 v1, v6, v1
	v_mul_lo_u32 v4, v1, v3
	v_sub_u32_e32 v4, v6, v4
	v_add_u32_e32 v5, 1, v1
	v_cmp_ge_u32_e32 vcc, v4, v3
	s_nop 1
	v_cndmask_b32_e32 v1, v1, v5, vcc
	v_sub_u32_e32 v5, v4, v3
	v_cndmask_b32_e32 v4, v4, v5, vcc
	v_add_u32_e32 v5, 1, v1
	v_cmp_ge_u32_e32 vcc, v4, v3
	v_add_u32_e32 v4, 1, v6
	s_nop 0
	v_cndmask_b32_e32 v1, v1, v5, vcc
	v_mul_lo_u32 v5, v3, v1
	v_add_u32_e32 v3, v5, v3
	v_cmp_ne_u32_e32 vcc, v4, v3
	s_and_saveexec_b64 s[4:5], vcc
	s_xor_b64 s[10:11], exec, s[4:5]
	s_cbranch_execz .LBB0_427
	v_readlane_b32 s4, v254, 49
	v_readlane_b32 s5, v254, 50
	s_waitcnt lgkmcnt(0)
	s_nop 3
	global_load_dword v2, v115, s[4:5] sc1
	s_waitcnt vmcnt(0)
	v_cmp_eq_u32_e32 vcc, v2, v1
	s_and_saveexec_b64 s[26:27], vcc
	s_cbranch_execz .LBB0_426
	s_mov_b32 s4, 1
	s_mov_b64 s[28:29], 0
	s_branch .LBB0_417

.LBB0_569:
	s_or_b64 exec, exec, s[10:11]
	v_cvt_f32_u32_e32 v5, v3
	s_waitcnt vmcnt(0)
	v_readfirstlane_b32 s4, v4
	v_sub_u32_e32 v4, 0, v3
	v_rcp_iflag_f32_e32 v5, v5
	v_add_u32_e32 v6, s4, v1
	v_mul_f32_e32 v5, 0x4f7ffffe, v5
	v_cvt_u32_f32_e32 v5, v5
	v_mul_lo_u32 v1, v4, v5
	v_mul_hi_u32 v1, v5, v1
	v_add_u32_e32 v1, v5, v1
	v_mul_hi_u32 v1, v6, v1
	v_mul_lo_u32 v4, v1, v3
	v_sub_u32_e32 v4, v6, v4
	v_add_u32_e32 v5, 1, v1
	v_cmp_ge_u32_e32 vcc, v4, v3
	s_nop 1
	v_cndmask_b32_e32 v1, v1, v5, vcc
	v_sub_u32_e32 v5, v4, v3
	v_cndmask_b32_e32 v4, v4, v5, vcc
	v_add_u32_e32 v5, 1, v1
	v_cmp_ge_u32_e32 vcc, v4, v3
	v_add_u32_e32 v4, 1, v6
	s_nop 0
	v_cndmask_b32_e32 v1, v1, v5, vcc
	v_mul_lo_u32 v5, v3, v1
	v_add_u32_e32 v3, v5, v3
	v_cmp_ne_u32_e32 vcc, v4, v3
	s_and_saveexec_b64 s[4:5], vcc
	s_xor_b64 s[10:11], exec, s[4:5]
	s_cbranch_execz .LBB0_583
	v_readlane_b32 s4, v254, 49
	v_readlane_b32 s5, v254, 50
	s_waitcnt lgkmcnt(0)
	s_nop 3
	global_load_dword v2, v115, s[4:5] sc1
	s_waitcnt vmcnt(0)
	v_cmp_eq_u32_e32 vcc, v2, v1
	s_and_saveexec_b64 s[28:29], vcc
	s_cbranch_execz .LBB0_582
	s_mov_b32 s4, 1
	s_mov_b64 s[38:39], 0
	s_branch .LBB0_573

.LBB0_1021:
	s_or_b64 exec, exec, s[4:5]
	v_cvt_f32_u32_e32 v5, v3
	s_waitcnt vmcnt(0)
	v_readfirstlane_b32 s4, v4
	v_sub_u32_e32 v4, 0, v3
	v_rcp_iflag_f32_e32 v5, v5
	v_add_u32_e32 v6, s4, v1
	v_mul_f32_e32 v5, 0x4f7ffffe, v5
	v_cvt_u32_f32_e32 v5, v5
	v_mul_lo_u32 v1, v4, v5
	v_mul_hi_u32 v1, v5, v1
	v_add_u32_e32 v1, v5, v1
	v_mul_hi_u32 v1, v6, v1
	v_mul_lo_u32 v4, v1, v3
	v_sub_u32_e32 v4, v6, v4
	v_add_u32_e32 v5, 1, v1
	v_cmp_ge_u32_e32 vcc, v4, v3
	s_nop 1
	v_cndmask_b32_e32 v1, v1, v5, vcc
	v_sub_u32_e32 v5, v4, v3
	v_cndmask_b32_e32 v4, v4, v5, vcc
	v_add_u32_e32 v5, 1, v1
	v_cmp_ge_u32_e32 vcc, v4, v3
	v_add_u32_e32 v4, 1, v6
	s_nop 0
	v_cndmask_b32_e32 v1, v1, v5, vcc
	v_mul_lo_u32 v5, v3, v1
	v_add_u32_e32 v3, v5, v3
	v_cmp_ne_u32_e32 vcc, v4, v3
	s_and_saveexec_b64 s[4:5], vcc
	s_xor_b64 s[4:5], exec, s[4:5]
	s_cbranch_execz .LBB0_1035
	v_readlane_b32 s8, v254, 49
	v_readlane_b32 s9, v254, 50
	s_waitcnt lgkmcnt(0)
	s_nop 3
	global_load_dword v2, v115, s[8:9] sc1
	s_waitcnt vmcnt(0)
	v_cmp_eq_u32_e32 vcc, v2, v1
	s_and_saveexec_b64 s[8:9], vcc
	s_cbranch_execz .LBB0_1034
	s_mov_b32 s7, 1
	s_mov_b64 s[10:11], 0
	s_branch .LBB0_1025

.LBB0_1124:
	s_or_b64 exec, exec, s[8:9]
	v_cvt_f32_u32_e32 v5, v3
	s_waitcnt vmcnt(0)
	v_readfirstlane_b32 s7, v4
	v_sub_u32_e32 v4, 0, v3
	v_rcp_iflag_f32_e32 v5, v5
	v_add_u32_e32 v6, s7, v1
	v_mul_f32_e32 v5, 0x4f7ffffe, v5
	v_cvt_u32_f32_e32 v5, v5
	v_mul_lo_u32 v1, v4, v5
	v_mul_hi_u32 v1, v5, v1
	v_add_u32_e32 v1, v5, v1
	v_mul_hi_u32 v1, v6, v1
	v_mul_lo_u32 v4, v1, v3
	v_sub_u32_e32 v4, v6, v4
	v_add_u32_e32 v5, 1, v1
	v_cmp_ge_u32_e32 vcc, v4, v3
	s_nop 1
	v_cndmask_b32_e32 v1, v1, v5, vcc
	v_sub_u32_e32 v5, v4, v3
	v_cndmask_b32_e32 v4, v4, v5, vcc
	v_add_u32_e32 v5, 1, v1
	v_cmp_ge_u32_e32 vcc, v4, v3
	v_add_u32_e32 v4, 1, v6
	s_nop 0
	v_cndmask_b32_e32 v1, v1, v5, vcc
	v_mul_lo_u32 v5, v3, v1
	v_add_u32_e32 v3, v5, v3
	v_cmp_ne_u32_e32 vcc, v4, v3
	s_and_saveexec_b64 s[8:9], vcc
	s_xor_b64 s[8:9], exec, s[8:9]
	s_cbranch_execz .LBB0_1138
	v_readlane_b32 s10, v254, 49
	v_readlane_b32 s11, v254, 50
	s_waitcnt lgkmcnt(0)
	s_nop 3
	global_load_dword v2, v115, s[10:11] sc1
	s_waitcnt vmcnt(0)
	v_cmp_eq_u32_e32 vcc, v2, v1
	s_and_saveexec_b64 s[10:11], vcc
	s_cbranch_execz .LBB0_1137
	s_mov_b32 s7, 1
	s_mov_b64 s[26:27], 0
	s_branch .LBB0_1128
